# P5 gate loads nt
# baseline (speedup 1.0000x reference)
.LBB0_760:
	s_cmpk_lg_i32 s26, 0x400
	s_cbranch_scc1 .LBB0_762
	v_mov_b32_e32 v130, 0
	s_nop 0
	v_add_u32_e32 v138, v130, v1
	v_add_u32_e32 v130, s13, v138
	v_ashrrev_i32_e32 v131, 31, v130
	v_lshlrev_b64 v[130:131], 10, v[130:131]
	v_lshl_add_u64 v[130:131], v[130:131], 0, v[208:209]
	v_lshlrev_b64 v[144:145], 1, v[130:131]
	v_lshl_add_u64 v[130:131], s[4:5], 0, v[144:145]
	global_load_dwordx4 v[134:137], v[130:131], off nt
	v_lshl_add_u64 v[130:131], s[2:3], 0, v[144:145]
	v_or_b32_e32 v144, 0x100, v144
	v_lshl_add_u64 v[140:141], s[4:5], 0, v[144:145]
	global_load_dwordx4 v[130:133], v[130:131], off nt
	v_lshl_add_u64 v[144:145], s[2:3], 0, v[144:145]
	global_load_dwordx4 v[140:143], v[140:141], off nt
	v_add_u32_e32 v148, s63, v138
	global_load_dwordx4 v[144:147], v[144:145], off nt
	v_ashrrev_i32_e32 v149, 31, v148
	v_lshlrev_b64 v[148:149], 10, v[148:149]
	v_lshl_add_u64 v[148:149], v[148:149], 0, v[208:209]
	v_lshlrev_b64 v[156:157], 1, v[148:149]
	v_lshl_add_u64 v[148:149], s[2:3], 0, v[156:157]
	v_lshl_add_u64 v[152:153], s[4:5], 0, v[156:157]
	global_load_dwordx4 v[148:151], v[148:149], off nt
	s_nop 0
	global_load_dwordx4 v[152:155], v[152:153], off nt
	v_or_b32_e32 v156, 0x100, v156
	v_lshl_add_u64 v[158:159], s[2:3], 0, v[156:157]
	v_lshl_add_u64 v[160:161], s[4:5], 0, v[156:157]
	global_load_dwordx4 v[156:159], v[158:159], off nt
	s_nop 0
	global_load_dwordx4 v[160:163], v[160:161], off nt
	s_waitcnt vmcnt(0)
	v_lshlrev_b32_e32 v139, 16, v134
	v_lshlrev_b32_e32 v168, 16, v135
	v_and_b32_e32 v169, 0xffff0000, v135
	v_rcp_f32_e32 v164, v139
	v_rcp_f32_e32 v168, v168
	v_rcp_f32_e32 v169, v169
	v_lshlrev_b32_e32 v139, 16, v140
	v_and_b32_e32 v173, 0xffff0000, v140
	v_rcp_f32_e32 v172, v139
	v_rcp_f32_e32 v173, v173
	v_and_b32_e32 v165, 0xffff0000, v134
	v_lshlrev_b32_e32 v134, 16, v130
	v_and_b32_e32 v135, 0xffff0000, v130
	v_lshlrev_b32_e32 v130, 16, v131
	v_and_b32_e32 v131, 0xffff0000, v131
	v_lshlrev_b32_e32 v176, 16, v141
	v_and_b32_e32 v177, 0xffff0000, v141
	v_lshlrev_b32_e32 v140, 16, v144
	v_and_b32_e32 v141, 0xffff0000, v144
	v_pk_mul_f32 v[130:131], v[168:169], v[130:131]
	v_lshlrev_b32_e32 v166, 16, v136
	v_and_b32_e32 v167, 0xffff0000, v136
	v_lshlrev_b32_e32 v170, 16, v137
	v_and_b32_e32 v171, 0xffff0000, v137
	v_rcp_f32_e32 v165, v165
	v_pk_mul_f32 v[128:129], v[128:129], v[130:131]
	v_pk_mul_f32 v[130:131], v[172:173], v[140:141]
	v_rcp_f32_e32 v166, v166
	v_rcp_f32_e32 v167, v167
	v_rcp_f32_e32 v170, v170
	v_rcp_f32_e32 v171, v171
	v_lshlrev_b32_e32 v174, 16, v142
	v_and_b32_e32 v175, 0xffff0000, v142
	v_lshlrev_b32_e32 v178, 16, v143
	v_and_b32_e32 v179, 0xffff0000, v143
	v_rcp_f32_e32 v176, v176
	v_rcp_f32_e32 v177, v177
	v_pk_mul_f32 v[94:95], v[94:95], v[130:131]
	v_add_u32_e32 v130, s64, v138
	v_rcp_f32_e32 v174, v174
	v_rcp_f32_e32 v175, v175
	v_rcp_f32_e32 v178, v178
	v_rcp_f32_e32 v179, v179
	v_ashrrev_i32_e32 v131, 31, v130
	v_lshlrev_b64 v[130:131], 10, v[130:131]
	v_lshlrev_b32_e32 v136, 16, v132
	v_and_b32_e32 v137, 0xffff0000, v132
	v_lshlrev_b32_e32 v132, 16, v133
	v_and_b32_e32 v133, 0xffff0000, v133
	v_lshlrev_b32_e32 v144, 16, v145
	v_and_b32_e32 v145, 0xffff0000, v145
	v_pk_mul_f32 v[134:135], v[164:165], v[134:135]
	v_lshl_add_u64 v[130:131], v[130:131], 0, v[208:209]
	v_lshlrev_b32_e32 v142, 16, v146
	v_and_b32_e32 v143, 0xffff0000, v146
	v_lshlrev_b32_e32 v146, 16, v147
	v_and_b32_e32 v147, 0xffff0000, v147
	v_pk_mul_f32 v[136:137], v[166:167], v[136:137]
	v_pk_mul_f32 v[132:133], v[170:171], v[132:133]
	v_pk_mul_f32 v[126:127], v[126:127], v[134:135]
	v_pk_mul_f32 v[134:135], v[176:177], v[144:145]
	v_lshlrev_b64 v[140:141], 1, v[130:131]
	v_pk_mul_f32 v[122:123], v[122:123], v[136:137]
	v_pk_mul_f32 v[124:125], v[124:125], v[132:133]
	v_pk_mul_f32 v[132:133], v[174:175], v[142:143]
	v_pk_mul_f32 v[136:137], v[178:179], v[146:147]
	v_pk_mul_f32 v[96:97], v[96:97], v[134:135]
	v_lshl_add_u64 v[130:131], s[2:3], 0, v[140:141]
	v_lshl_add_u64 v[134:135], s[4:5], 0, v[140:141]
	v_pk_mul_f32 v[90:91], v[90:91], v[132:133]
	v_pk_mul_f32 v[92:93], v[92:93], v[136:137]
	global_load_dwordx4 v[130:133], v[130:131], off nt
	s_nop 0
	global_load_dwordx4 v[134:137], v[134:135], off nt
	v_lshlrev_b32_e32 v139, 16, v152
	v_and_b32_e32 v143, 0xffff0000, v152
	v_rcp_f32_e32 v142, v139
	v_rcp_f32_e32 v143, v143
	v_lshlrev_b32_e32 v144, 16, v154
	v_and_b32_e32 v145, 0xffff0000, v154
	v_rcp_f32_e32 v144, v144
	v_rcp_f32_e32 v145, v145
	v_lshlrev_b32_e32 v146, 16, v148
	v_and_b32_e32 v147, 0xffff0000, v148
	v_pk_mul_f32 v[142:143], v[142:143], v[146:147]
	v_lshlrev_b32_e32 v152, 16, v153
	v_pk_mul_f32 v[118:119], v[118:119], v[142:143]
	v_lshlrev_b32_e32 v142, 16, v150
	v_and_b32_e32 v143, 0xffff0000, v150
	v_and_b32_e32 v153, 0xffff0000, v153
	v_pk_mul_f32 v[142:143], v[144:145], v[142:143]
	v_lshlrev_b32_e32 v154, 16, v155
	v_pk_mul_f32 v[114:115], v[114:115], v[142:143]
	v_rcp_f32_e32 v142, v152
	v_rcp_f32_e32 v143, v153
	v_and_b32_e32 v155, 0xffff0000, v155
	v_rcp_f32_e32 v144, v154
	v_rcp_f32_e32 v145, v155
	v_lshlrev_b32_e32 v146, 16, v149
	v_and_b32_e32 v147, 0xffff0000, v149
	v_pk_mul_f32 v[142:143], v[142:143], v[146:147]
	v_or_b32_e32 v140, 0x100, v140
	v_pk_mul_f32 v[120:121], v[120:121], v[142:143]
	v_lshlrev_b32_e32 v142, 16, v151
	v_and_b32_e32 v143, 0xffff0000, v151
	v_pk_mul_f32 v[142:143], v[144:145], v[142:143]
	v_lshl_add_u64 v[144:145], s[4:5], 0, v[140:141]
	v_pk_mul_f32 v[116:117], v[116:117], v[142:143]
	v_lshl_add_u64 v[142:143], s[2:3], 0, v[140:141]
	v_lshlrev_b32_e32 v139, 16, v160
	v_and_b32_e32 v149, 0xffff0000, v160
	global_load_dwordx4 v[140:143], v[142:143], off nt
	s_nop 0
	global_load_dwordx4 v[144:147], v[144:145], off nt
	v_rcp_f32_e32 v148, v139
	v_rcp_f32_e32 v149, v149
	v_lshlrev_b32_e32 v150, 16, v162
	v_and_b32_e32 v151, 0xffff0000, v162
	v_rcp_f32_e32 v150, v150
	v_rcp_f32_e32 v151, v151
	v_lshlrev_b32_e32 v152, 16, v156
	v_and_b32_e32 v153, 0xffff0000, v156
	v_pk_mul_f32 v[148:149], v[148:149], v[152:153]
	v_lshlrev_b32_e32 v154, 16, v161
	v_pk_mul_f32 v[86:87], v[86:87], v[148:149]
	v_lshlrev_b32_e32 v148, 16, v158
	v_and_b32_e32 v149, 0xffff0000, v158
	v_and_b32_e32 v155, 0xffff0000, v161
	v_pk_mul_f32 v[148:149], v[150:151], v[148:149]
	v_lshlrev_b32_e32 v160, 16, v163
	v_pk_mul_f32 v[82:83], v[82:83], v[148:149]
	v_rcp_f32_e32 v148, v154
	v_rcp_f32_e32 v149, v155
	v_and_b32_e32 v161, 0xffff0000, v163
	v_rcp_f32_e32 v150, v160
	v_rcp_f32_e32 v151, v161
	v_lshlrev_b32_e32 v152, 16, v157
	v_and_b32_e32 v153, 0xffff0000, v157
	v_pk_mul_f32 v[148:149], v[148:149], v[152:153]
	s_waitcnt vmcnt(0)
	v_lshlrev_b32_e32 v139, 16, v134
	v_pk_mul_f32 v[88:89], v[88:89], v[148:149]
	v_lshlrev_b32_e32 v148, 16, v159
	v_and_b32_e32 v149, 0xffff0000, v159
	v_pk_mul_f32 v[148:149], v[150:151], v[148:149]
	v_and_b32_e32 v158, 0xffff0000, v134
	v_pk_mul_f32 v[84:85], v[84:85], v[148:149]
	v_add_u32_e32 v148, s65, v138
	v_ashrrev_i32_e32 v149, 31, v148
	v_lshlrev_b64 v[148:149], 10, v[148:149]
	v_lshl_add_u64 v[148:149], v[148:149], 0, v[208:209]
	v_lshlrev_b64 v[156:157], 1, v[148:149]
	v_lshl_add_u64 v[148:149], s[2:3], 0, v[156:157]
	v_lshl_add_u64 v[152:153], s[4:5], 0, v[156:157]
	global_load_dwordx4 v[148:151], v[148:149], off nt
	s_nop 0
	global_load_dwordx4 v[152:155], v[152:153], off nt
	v_lshlrev_b32_e32 v160, 16, v135
	v_and_b32_e32 v161, 0xffff0000, v135
	v_rcp_f32_e32 v134, v139
	v_rcp_f32_e32 v135, v158
	v_lshlrev_b32_e32 v159, 16, v136
	v_and_b32_e32 v162, 0xffff0000, v136
	v_lshlrev_b32_e32 v163, 16, v137
	v_and_b32_e32 v164, 0xffff0000, v137
	v_rcp_f32_e32 v136, v159
	v_rcp_f32_e32 v137, v162
	v_lshlrev_b32_e32 v158, 16, v130
	v_and_b32_e32 v159, 0xffff0000, v130
	v_pk_mul_f32 v[134:135], v[134:135], v[158:159]
	v_rcp_f32_e32 v130, v163
	v_pk_mul_f32 v[110:111], v[110:111], v[134:135]
	v_lshlrev_b32_e32 v134, 16, v132
	v_and_b32_e32 v135, 0xffff0000, v132
	v_pk_mul_f32 v[134:135], v[136:137], v[134:135]
	v_lshlrev_b32_e32 v136, 16, v131
	v_pk_mul_f32 v[106:107], v[106:107], v[134:135]
	v_rcp_f32_e32 v134, v160
	v_rcp_f32_e32 v135, v161
	v_and_b32_e32 v137, 0xffff0000, v131
	v_rcp_f32_e32 v131, v164
	v_lshlrev_b32_e32 v132, 16, v133
	v_and_b32_e32 v133, 0xffff0000, v133
	v_pk_mul_f32 v[134:135], v[134:135], v[136:137]
	v_pk_mul_f32 v[130:131], v[130:131], v[132:133]
	v_or_b32_e32 v156, 0x100, v156
	v_pk_mul_f32 v[112:113], v[112:113], v[134:135]
	v_pk_mul_f32 v[108:109], v[108:109], v[130:131]
	v_lshl_add_u64 v[130:131], s[2:3], 0, v[156:157]
	v_lshl_add_u64 v[134:135], s[4:5], 0, v[156:157]
	global_load_dwordx4 v[130:133], v[130:131], off nt
	s_nop 0
	global_load_dwordx4 v[134:137], v[134:135], off nt
	v_lshlrev_b32_e32 v139, 16, v144
	v_and_b32_e32 v156, 0xffff0000, v144
	v_lshlrev_b32_e32 v158, 16, v145
	v_and_b32_e32 v159, 0xffff0000, v145
	v_rcp_f32_e32 v144, v139
	v_rcp_f32_e32 v145, v156
	v_lshlrev_b32_e32 v157, 16, v146
	v_and_b32_e32 v160, 0xffff0000, v146
	v_lshlrev_b32_e32 v161, 16, v147
	v_and_b32_e32 v162, 0xffff0000, v147
	v_rcp_f32_e32 v146, v157
	v_rcp_f32_e32 v147, v160
	v_lshlrev_b32_e32 v156, 16, v140
	v_and_b32_e32 v157, 0xffff0000, v140
	v_pk_mul_f32 v[144:145], v[144:145], v[156:157]
	v_rcp_f32_e32 v140, v161
	v_pk_mul_f32 v[78:79], v[78:79], v[144:145]
	v_lshlrev_b32_e32 v144, 16, v142
	v_and_b32_e32 v145, 0xffff0000, v142
	v_pk_mul_f32 v[144:145], v[146:147], v[144:145]
	v_lshlrev_b32_e32 v146, 16, v141
	v_and_b32_e32 v147, 0xffff0000, v141
	v_rcp_f32_e32 v141, v162
	v_lshlrev_b32_e32 v142, 16, v143
	v_and_b32_e32 v143, 0xffff0000, v143
	v_pk_mul_f32 v[74:75], v[74:75], v[144:145]
	v_pk_mul_f32 v[140:141], v[140:141], v[142:143]
	v_rcp_f32_e32 v144, v158
	v_rcp_f32_e32 v145, v159
	v_pk_mul_f32 v[76:77], v[76:77], v[140:141]
	v_add_u32_e32 v140, s66, v138
	v_ashrrev_i32_e32 v141, 31, v140
	v_lshlrev_b64 v[140:141], 10, v[140:141]
	v_lshl_add_u64 v[140:141], v[140:141], 0, v[208:209]
	v_pk_mul_f32 v[144:145], v[144:145], v[146:147]
	v_lshlrev_b64 v[156:157], 1, v[140:141]
	v_pk_mul_f32 v[80:81], v[80:81], v[144:145]
	v_lshl_add_u64 v[140:141], s[2:3], 0, v[156:157]
	v_lshl_add_u64 v[144:145], s[4:5], 0, v[156:157]
	global_load_dwordx4 v[140:143], v[140:141], off nt
	s_nop 0
	global_load_dwordx4 v[144:147], v[144:145], off nt
	v_or_b32_e32 v156, 0x100, v156
	s_waitcnt vmcnt(0)
	v_lshlrev_b32_e32 v139, 16, v152
	v_and_b32_e32 v158, 0xffff0000, v152
	v_lshlrev_b32_e32 v160, 16, v153
	v_and_b32_e32 v161, 0xffff0000, v153
	v_rcp_f32_e32 v152, v139
	v_rcp_f32_e32 v153, v158
	v_lshlrev_b32_e32 v159, 16, v154
	v_and_b32_e32 v162, 0xffff0000, v154
	v_lshlrev_b32_e32 v163, 16, v155
	v_and_b32_e32 v164, 0xffff0000, v155
	v_rcp_f32_e32 v154, v159
	v_rcp_f32_e32 v155, v162
	v_lshlrev_b32_e32 v158, 16, v148
	v_and_b32_e32 v159, 0xffff0000, v148
	v_pk_mul_f32 v[152:153], v[152:153], v[158:159]
	v_rcp_f32_e32 v148, v163
	v_pk_mul_f32 v[102:103], v[102:103], v[152:153]
	v_lshlrev_b32_e32 v152, 16, v150
	v_and_b32_e32 v153, 0xffff0000, v150
	v_pk_mul_f32 v[152:153], v[154:155], v[152:153]
	v_lshlrev_b32_e32 v154, 16, v149
	v_pk_mul_f32 v[98:99], v[98:99], v[152:153]
	v_rcp_f32_e32 v152, v160
	v_rcp_f32_e32 v153, v161
	v_and_b32_e32 v155, 0xffff0000, v149
	v_rcp_f32_e32 v149, v164
	v_lshlrev_b32_e32 v150, 16, v151
	v_and_b32_e32 v151, 0xffff0000, v151
	v_pk_mul_f32 v[152:153], v[152:153], v[154:155]
	v_pk_mul_f32 v[148:149], v[148:149], v[150:151]
	v_pk_mul_f32 v[104:105], v[104:105], v[152:153]
	v_pk_mul_f32 v[100:101], v[100:101], v[148:149]
	v_lshl_add_u64 v[148:149], s[2:3], 0, v[156:157]
	v_lshl_add_u64 v[152:153], s[4:5], 0, v[156:157]
	global_load_dwordx4 v[148:151], v[148:149], off nt
	s_nop 0
	global_load_dwordx4 v[152:155], v[152:153], off nt
	v_lshlrev_b32_e32 v139, 16, v134
	v_and_b32_e32 v156, 0xffff0000, v134
	v_lshlrev_b32_e32 v158, 16, v135
	v_and_b32_e32 v159, 0xffff0000, v135
	v_rcp_f32_e32 v134, v139
	v_rcp_f32_e32 v135, v156
	v_lshlrev_b32_e32 v157, 16, v136
	v_and_b32_e32 v160, 0xffff0000, v136
	v_lshlrev_b32_e32 v161, 16, v137
	v_and_b32_e32 v162, 0xffff0000, v137
	v_rcp_f32_e32 v136, v157
	v_rcp_f32_e32 v137, v160
	v_lshlrev_b32_e32 v156, 16, v130
	v_and_b32_e32 v157, 0xffff0000, v130
	v_pk_mul_f32 v[134:135], v[134:135], v[156:157]
	v_rcp_f32_e32 v130, v161
	v_pk_mul_f32 v[70:71], v[70:71], v[134:135]
	v_lshlrev_b32_e32 v134, 16, v132
	v_and_b32_e32 v135, 0xffff0000, v132
	v_pk_mul_f32 v[134:135], v[136:137], v[134:135]
	v_lshlrev_b32_e32 v136, 16, v131
	v_and_b32_e32 v137, 0xffff0000, v131
	v_rcp_f32_e32 v131, v162
	v_lshlrev_b32_e32 v132, 16, v133
	v_and_b32_e32 v133, 0xffff0000, v133
	v_pk_mul_f32 v[66:67], v[66:67], v[134:135]
	v_pk_mul_f32 v[130:131], v[130:131], v[132:133]
	v_rcp_f32_e32 v134, v158
	v_pk_mul_f32 v[68:69], v[68:69], v[130:131]
	v_add_u32_e32 v130, s67, v138
	v_rcp_f32_e32 v135, v159
	v_ashrrev_i32_e32 v131, 31, v130
	v_lshlrev_b64 v[130:131], 10, v[130:131]
	v_lshl_add_u64 v[130:131], v[130:131], 0, v[208:209]
	v_lshlrev_b64 v[130:131], 1, v[130:131]
	v_pk_mul_f32 v[134:135], v[134:135], v[136:137]
	v_lshl_add_u64 v[132:133], s[2:3], 0, v[130:131]
	v_pk_mul_f32 v[72:73], v[72:73], v[134:135]
	v_lshl_add_u64 v[134:135], s[4:5], 0, v[130:131]
	global_load_dwordx4 v[156:159], v[132:133], off nt
	global_load_dwordx4 v[160:163], v[134:135], off nt
	v_lshlrev_b32_e32 v132, 16, v144
	v_and_b32_e32 v133, 0xffff0000, v144
	v_rcp_f32_e32 v132, v132
	v_rcp_f32_e32 v133, v133
	v_lshlrev_b32_e32 v134, 16, v146
	v_and_b32_e32 v135, 0xffff0000, v146
	v_rcp_f32_e32 v134, v134
	v_rcp_f32_e32 v135, v135
	v_lshlrev_b32_e32 v136, 16, v140
	v_and_b32_e32 v137, 0xffff0000, v140
	v_pk_mul_f32 v[132:133], v[132:133], v[136:137]
	v_lshlrev_b32_e32 v139, 16, v145
	v_pk_mul_f32 v[62:63], v[62:63], v[132:133]
	v_lshlrev_b32_e32 v132, 16, v142
	v_and_b32_e32 v133, 0xffff0000, v142
	v_and_b32_e32 v144, 0xffff0000, v145
	v_pk_mul_f32 v[132:133], v[134:135], v[132:133]
	v_lshlrev_b32_e32 v145, 16, v147
	v_pk_mul_f32 v[58:59], v[58:59], v[132:133]
	v_rcp_f32_e32 v132, v139
	v_rcp_f32_e32 v133, v144
	v_and_b32_e32 v146, 0xffff0000, v147
	v_rcp_f32_e32 v134, v145
	v_rcp_f32_e32 v135, v146
	v_lshlrev_b32_e32 v136, 16, v141
	v_and_b32_e32 v137, 0xffff0000, v141
	v_pk_mul_f32 v[132:133], v[132:133], v[136:137]
	v_or_b32_e32 v130, 0x100, v130
	v_pk_mul_f32 v[64:65], v[64:65], v[132:133]
	v_lshlrev_b32_e32 v132, 16, v143
	v_and_b32_e32 v133, 0xffff0000, v143
	v_pk_mul_f32 v[132:133], v[134:135], v[132:133]
	v_lshl_add_u64 v[134:135], s[4:5], 0, v[130:131]
	v_pk_mul_f32 v[60:61], v[60:61], v[132:133]
	v_lshl_add_u64 v[132:133], s[2:3], 0, v[130:131]
	global_load_dwordx4 v[130:133], v[132:133], off nt
	s_nop 0
	global_load_dwordx4 v[140:143], v[134:135], off nt
	s_waitcnt vmcnt(0)
	v_lshlrev_b32_e32 v144, 16, v148
	v_lshlrev_b32_e32 v134, 16, v152
	v_and_b32_e32 v135, 0xffff0000, v152
	v_rcp_f32_e32 v134, v134
	v_rcp_f32_e32 v135, v135
	v_lshlrev_b32_e32 v136, 16, v154
	v_and_b32_e32 v137, 0xffff0000, v154
	v_rcp_f32_e32 v136, v136
	v_rcp_f32_e32 v137, v137
	v_and_b32_e32 v145, 0xffff0000, v148
	v_pk_mul_f32 v[134:135], v[134:135], v[144:145]
	v_lshlrev_b32_e32 v139, 16, v153
	v_pk_mul_f32 v[30:31], v[30:31], v[134:135]
	v_lshlrev_b32_e32 v134, 16, v150
	v_and_b32_e32 v135, 0xffff0000, v150
	v_and_b32_e32 v146, 0xffff0000, v153
	v_pk_mul_f32 v[134:135], v[136:137], v[134:135]
	v_lshlrev_b32_e32 v147, 16, v155
	v_pk_mul_f32 v[26:27], v[26:27], v[134:135]
	v_rcp_f32_e32 v134, v139
	v_rcp_f32_e32 v135, v146
	v_and_b32_e32 v152, 0xffff0000, v155
	v_rcp_f32_e32 v136, v147
	v_rcp_f32_e32 v137, v152
	v_lshlrev_b32_e32 v144, 16, v149
	v_and_b32_e32 v145, 0xffff0000, v149
	v_pk_mul_f32 v[134:135], v[134:135], v[144:145]
	v_lshlrev_b32_e32 v154, 16, v156
	v_pk_mul_f32 v[32:33], v[32:33], v[134:135]
	v_lshlrev_b32_e32 v134, 16, v151
	v_and_b32_e32 v135, 0xffff0000, v151
	v_pk_mul_f32 v[134:135], v[136:137], v[134:135]
	v_lshlrev_b32_e32 v139, 16, v160
	v_pk_mul_f32 v[28:29], v[28:29], v[134:135]
	v_add_u32_e32 v134, s68, v138
	v_ashrrev_i32_e32 v135, 31, v134
	v_lshlrev_b64 v[134:135], 10, v[134:135]
	v_lshl_add_u64 v[134:135], v[134:135], 0, v[208:209]
	v_lshlrev_b64 v[148:149], 1, v[134:135]
	v_lshl_add_u64 v[134:135], s[2:3], 0, v[148:149]
	v_lshl_add_u64 v[144:145], s[4:5], 0, v[148:149]
	global_load_dwordx4 v[134:137], v[134:135], off nt
	s_nop 0
	global_load_dwordx4 v[144:147], v[144:145], off nt
	v_and_b32_e32 v151, 0xffff0000, v160
	v_rcp_f32_e32 v150, v139
	v_rcp_f32_e32 v151, v151
	v_lshlrev_b32_e32 v152, 16, v162
	v_and_b32_e32 v153, 0xffff0000, v162
	v_rcp_f32_e32 v152, v152
	v_rcp_f32_e32 v153, v153
	v_and_b32_e32 v155, 0xffff0000, v156
	v_pk_mul_f32 v[150:151], v[150:151], v[154:155]
	v_lshlrev_b32_e32 v160, 16, v161
	v_pk_mul_f32 v[54:55], v[54:55], v[150:151]
	v_lshlrev_b32_e32 v150, 16, v158
	v_and_b32_e32 v151, 0xffff0000, v158
	v_and_b32_e32 v161, 0xffff0000, v161
	v_pk_mul_f32 v[150:151], v[152:153], v[150:151]
	v_lshlrev_b32_e32 v162, 16, v163
	v_pk_mul_f32 v[50:51], v[50:51], v[150:151]
	v_rcp_f32_e32 v150, v160
	v_rcp_f32_e32 v151, v161
	v_and_b32_e32 v163, 0xffff0000, v163
	v_rcp_f32_e32 v152, v162
	v_rcp_f32_e32 v153, v163
	v_lshlrev_b32_e32 v154, 16, v157
	v_and_b32_e32 v155, 0xffff0000, v157
	v_pk_mul_f32 v[150:151], v[150:151], v[154:155]
	v_or_b32_e32 v148, 0x100, v148
	v_pk_mul_f32 v[56:57], v[56:57], v[150:151]
	v_lshlrev_b32_e32 v150, 16, v159
	v_and_b32_e32 v151, 0xffff0000, v159
	v_pk_mul_f32 v[150:151], v[152:153], v[150:151]
	v_lshl_add_u64 v[152:153], s[4:5], 0, v[148:149]
	v_pk_mul_f32 v[52:53], v[52:53], v[150:151]
	v_lshl_add_u64 v[150:151], s[2:3], 0, v[148:149]
	global_load_dwordx4 v[148:151], v[150:151], off nt
	s_nop 0
	global_load_dwordx4 v[152:155], v[152:153], off nt
	v_lshlrev_b32_e32 v139, 16, v140
	v_and_b32_e32 v156, 0xffff0000, v140
	v_lshlrev_b32_e32 v158, 16, v141
	v_and_b32_e32 v159, 0xffff0000, v141
	v_rcp_f32_e32 v140, v139
	v_rcp_f32_e32 v141, v156
	v_lshlrev_b32_e32 v157, 16, v142
	v_and_b32_e32 v160, 0xffff0000, v142
	v_add_u32_e32 v138, s69, v138
	v_lshlrev_b32_e32 v162, 16, v143
	v_and_b32_e32 v164, 0xffff0000, v143
	v_rcp_f32_e32 v142, v157
	v_rcp_f32_e32 v143, v160
	v_ashrrev_i32_e32 v139, 31, v138
	v_lshlrev_b32_e32 v156, 16, v130
	v_and_b32_e32 v157, 0xffff0000, v130
	v_lshlrev_b64 v[138:139], 10, v[138:139]
	v_pk_mul_f32 v[140:141], v[140:141], v[156:157]
	v_lshl_add_u64 v[138:139], v[138:139], 0, v[208:209]
	v_pk_mul_f32 v[22:23], v[22:23], v[140:141]
	v_lshlrev_b32_e32 v140, 16, v132
	v_and_b32_e32 v141, 0xffff0000, v132
	v_lshlrev_b64 v[160:161], 1, v[138:139]
	v_pk_mul_f32 v[140:141], v[142:143], v[140:141]
	v_lshl_add_u64 v[138:139], s[2:3], 0, v[160:161]
	v_lshl_add_u64 v[156:157], s[4:5], 0, v[160:161]
	v_pk_mul_f32 v[18:19], v[18:19], v[140:141]
	v_rcp_f32_e32 v142, v158
	v_rcp_f32_e32 v143, v159
	global_load_dwordx4 v[138:141], v[138:139], off nt
	s_nop 0
	global_load_dwordx4 v[156:159], v[156:157], off nt
	v_rcp_f32_e32 v130, v162
	v_lshlrev_b32_e32 v162, 16, v131
	v_and_b32_e32 v163, 0xffff0000, v131
	v_rcp_f32_e32 v131, v164
	v_lshlrev_b32_e32 v132, 16, v133
	v_and_b32_e32 v133, 0xffff0000, v133
	v_pk_mul_f32 v[142:143], v[142:143], v[162:163]
	v_pk_mul_f32 v[130:131], v[130:131], v[132:133]
	v_pk_mul_f32 v[24:25], v[24:25], v[142:143]
	v_pk_mul_f32 v[20:21], v[20:21], v[130:131]
	v_or_b32_e32 v160, 0x100, v160
	s_waitcnt vmcnt(0)
	v_and_b32_e32 v133, 0xffff0000, v134
	v_lshlrev_b32_e32 v130, 16, v144
	v_and_b32_e32 v131, 0xffff0000, v144
	v_rcp_f32_e32 v130, v130
	v_rcp_f32_e32 v131, v131
	v_lshlrev_b32_e32 v132, 16, v146
	v_and_b32_e32 v142, 0xffff0000, v146
	v_rcp_f32_e32 v146, v132
	v_lshlrev_b32_e32 v132, 16, v134
	v_pk_mul_f32 v[130:131], v[130:131], v[132:133]
	v_lshlrev_b32_e32 v166, 16, v147
	v_and_b32_e32 v167, 0xffff0000, v147
	v_pk_mul_f32 v[46:47], v[46:47], v[130:131]
	v_rcp_f32_e32 v147, v142
	v_lshl_add_u64 v[130:131], s[2:3], 0, v[160:161]
	v_lshl_add_u64 v[142:143], s[4:5], 0, v[160:161]
	v_lshlrev_b32_e32 v164, 16, v145
	v_and_b32_e32 v165, 0xffff0000, v145
	global_load_dwordx4 v[130:133], v[130:131], off nt
	s_nop 0
	global_load_dwordx4 v[142:145], v[142:143], off nt
	v_rcp_f32_e32 v134, v166
	v_lshlrev_b32_e32 v160, 16, v135
	v_and_b32_e32 v161, 0xffff0000, v135
	v_rcp_f32_e32 v135, v167
	v_lshlrev_b32_e32 v162, 16, v136
	v_and_b32_e32 v163, 0xffff0000, v136
	v_pk_mul_f32 v[146:147], v[146:147], v[162:163]
	v_lshlrev_b32_e32 v136, 16, v137
	v_and_b32_e32 v137, 0xffff0000, v137
	v_pk_mul_f32 v[42:43], v[42:43], v[146:147]
	v_rcp_f32_e32 v146, v164
	v_rcp_f32_e32 v147, v165
	v_pk_mul_f32 v[134:135], v[134:135], v[136:137]
	v_pk_mul_f32 v[146:147], v[146:147], v[160:161]
	v_pk_mul_f32 v[44:45], v[44:45], v[134:135]
	v_lshlrev_b32_e32 v134, 16, v152
	v_and_b32_e32 v135, 0xffff0000, v152
	v_rcp_f32_e32 v134, v134
	v_rcp_f32_e32 v135, v135
	v_lshlrev_b32_e32 v136, 16, v154
	v_and_b32_e32 v137, 0xffff0000, v154
	v_rcp_f32_e32 v136, v136
	v_rcp_f32_e32 v137, v137
	v_pk_mul_f32 v[48:49], v[48:49], v[146:147]
	v_lshlrev_b32_e32 v146, 16, v148
	v_and_b32_e32 v147, 0xffff0000, v148
	v_pk_mul_f32 v[134:135], v[134:135], v[146:147]
	v_lshlrev_b32_e32 v152, 16, v153
	v_pk_mul_f32 v[14:15], v[14:15], v[134:135]
	v_lshlrev_b32_e32 v134, 16, v150
	v_and_b32_e32 v135, 0xffff0000, v150
	v_and_b32_e32 v153, 0xffff0000, v153
	v_pk_mul_f32 v[134:135], v[136:137], v[134:135]
	v_lshlrev_b32_e32 v154, 16, v155
	v_pk_mul_f32 v[10:11], v[10:11], v[134:135]
	v_rcp_f32_e32 v134, v152
	v_rcp_f32_e32 v135, v153
	v_and_b32_e32 v155, 0xffff0000, v155
	v_rcp_f32_e32 v136, v154
	v_rcp_f32_e32 v137, v155
	v_lshlrev_b32_e32 v146, 16, v149
	v_and_b32_e32 v147, 0xffff0000, v149
	v_pk_mul_f32 v[134:135], v[134:135], v[146:147]
	v_lshlrev_b32_e32 v146, 16, v138
	v_pk_mul_f32 v[16:17], v[16:17], v[134:135]
	v_lshlrev_b32_e32 v134, 16, v151
	v_and_b32_e32 v135, 0xffff0000, v151
	v_pk_mul_f32 v[134:135], v[136:137], v[134:135]
	v_lshlrev_b32_e32 v136, 16, v158
	v_pk_mul_f32 v[12:13], v[12:13], v[134:135]
	v_lshlrev_b32_e32 v134, 16, v156
	v_and_b32_e32 v135, 0xffff0000, v156
	v_rcp_f32_e32 v134, v134
	v_rcp_f32_e32 v135, v135
	v_and_b32_e32 v137, 0xffff0000, v158
	v_rcp_f32_e32 v136, v136
	v_rcp_f32_e32 v137, v137
	v_and_b32_e32 v147, 0xffff0000, v138
	v_pk_mul_f32 v[134:135], v[134:135], v[146:147]
	v_lshlrev_b32_e32 v148, 16, v157
	v_pk_mul_f32 v[38:39], v[38:39], v[134:135]
	v_lshlrev_b32_e32 v134, 16, v140
	v_and_b32_e32 v135, 0xffff0000, v140
	v_and_b32_e32 v149, 0xffff0000, v157
	v_pk_mul_f32 v[134:135], v[136:137], v[134:135]
	v_lshlrev_b32_e32 v150, 16, v159
	v_pk_mul_f32 v[34:35], v[34:35], v[134:135]
	v_rcp_f32_e32 v134, v148
	v_rcp_f32_e32 v135, v149
	v_and_b32_e32 v151, 0xffff0000, v159
	v_rcp_f32_e32 v136, v150
	v_rcp_f32_e32 v137, v151
	v_lshlrev_b32_e32 v138, 16, v139
	v_and_b32_e32 v139, 0xffff0000, v139
	v_pk_mul_f32 v[134:135], v[134:135], v[138:139]
	s_waitcnt vmcnt(0)
	v_lshlrev_b32_e32 v138, 16, v130
	v_pk_mul_f32 v[40:41], v[40:41], v[134:135]
	v_lshlrev_b32_e32 v134, 16, v141
	v_and_b32_e32 v135, 0xffff0000, v141
	v_pk_mul_f32 v[134:135], v[136:137], v[134:135]
	v_lshlrev_b32_e32 v136, 16, v144
	v_pk_mul_f32 v[36:37], v[36:37], v[134:135]
	v_lshlrev_b32_e32 v134, 16, v142
	v_and_b32_e32 v135, 0xffff0000, v142
	v_rcp_f32_e32 v134, v134
	v_rcp_f32_e32 v135, v135
	v_and_b32_e32 v137, 0xffff0000, v144
	v_rcp_f32_e32 v136, v136
	v_rcp_f32_e32 v137, v137
	v_and_b32_e32 v139, 0xffff0000, v130
	v_pk_mul_f32 v[134:135], v[134:135], v[138:139]
	v_lshlrev_b32_e32 v140, 16, v143
	v_pk_mul_f32 v[6:7], v[6:7], v[134:135]
	v_lshlrev_b32_e32 v134, 16, v132
	v_and_b32_e32 v135, 0xffff0000, v132
	v_and_b32_e32 v141, 0xffff0000, v143
	v_lshlrev_b32_e32 v142, 16, v145
	v_and_b32_e32 v143, 0xffff0000, v145
	v_pk_mul_f32 v[134:135], v[136:137], v[134:135]
	v_rcp_f32_e32 v130, v142
	v_pk_mul_f32 v[2:3], v[2:3], v[134:135]
	v_rcp_f32_e32 v134, v140
	v_rcp_f32_e32 v135, v141
	v_lshlrev_b32_e32 v136, 16, v131
	v_and_b32_e32 v137, 0xffff0000, v131
	v_rcp_f32_e32 v131, v143
	v_lshlrev_b32_e32 v132, 16, v133
	v_and_b32_e32 v133, 0xffff0000, v133
	v_pk_mul_f32 v[134:135], v[134:135], v[136:137]
	v_pk_mul_f32 v[130:131], v[130:131], v[132:133]
	v_pk_mul_f32 v[8:9], v[8:9], v[134:135]
	v_pk_mul_f32 v[4:5], v[4:5], v[130:131]

.LBB0_772:
	v_add_u32_e32 v130, s13, v1
	v_ashrrev_i32_e32 v131, 31, v130
	v_lshlrev_b64 v[130:131], 10, v[130:131]
	v_lshl_add_u64 v[130:131], v[130:131], 0, s[24:25]
	v_or_b32_e32 v130, v130, v202
	v_lshlrev_b64 v[130:131], 1, v[130:131]
	v_lshl_add_u64 v[132:133], s[4:5], 0, v[130:131]
	global_load_dwordx4 v[168:171], v[132:133], off nt
	global_load_dwordx4 v[172:175], v[132:133], off offset:256 nt
	v_add_co_u32_e32 v134, vcc, s56, v132
	v_lshl_add_u64 v[166:167], s[6:7], 0, v[130:131]
	s_nop 0
	v_addc_co_u32_e32 v135, vcc, 0, v133, vcc
	global_load_dwordx4 v[176:179], v[134:135], off nt
	v_add_co_u32_e32 v130, vcc, s52, v132
	s_waitcnt vmcnt(0)
	v_lshlrev_b32_e32 v192, 16, v168
	v_addc_co_u32_e32 v131, vcc, 0, v133, vcc
	v_add_co_u32_e32 v136, vcc, s55, v132
	v_and_b32_e32 v193, 0xffff0000, v168
	s_nop 0
	v_addc_co_u32_e32 v137, vcc, 0, v133, vcc
	global_load_dwordx4 v[180:183], v[130:131], off nt
	global_load_dwordx4 v[184:187], v[130:131], off offset:256 nt
	global_load_dwordx4 v[188:191], v[136:137], off nt
	global_load_dwordx4 v[162:165], v[136:137], off offset:256 nt
	global_load_dwordx4 v[208:211], v[134:135], off offset:256 nt
	v_add_co_u32_e32 v130, vcc, s57, v132
	v_lshlrev_b32_e32 v212, 16, v170
	s_nop 0
	v_addc_co_u32_e32 v131, vcc, 0, v133, vcc
	global_load_dwordx4 v[158:161], v[130:131], off nt
	global_load_dwordx4 v[154:157], v[130:131], off offset:256 nt
	v_add_co_u32_e32 v134, vcc, s58, v132
	v_and_b32_e32 v213, 0xffff0000, v170
	s_nop 0
	v_addc_co_u32_e32 v135, vcc, 0, v133, vcc
	global_load_dwordx4 v[150:153], v[134:135], off nt
	global_load_dwordx4 v[146:149], v[134:135], off offset:256 nt
	v_add_co_u32_e32 v130, vcc, s59, v132
	v_lshlrev_b32_e32 v168, 16, v169
	s_nop 0
	v_addc_co_u32_e32 v131, vcc, 0, v133, vcc
	global_load_dwordx4 v[142:145], v[130:131], off nt
	global_load_dwordx4 v[138:141], v[130:131], off offset:256 nt
	v_add_co_u32_e32 v132, vcc, s60, v132
	v_and_b32_e32 v169, 0xffff0000, v169
	s_nop 0
	v_addc_co_u32_e32 v133, vcc, 0, v133, vcc
	global_load_dwordx4 v[134:137], v[132:133], off nt
	s_nop 0
	global_load_dwordx4 v[130:133], v[132:133], off offset:256 nt
	v_lshlrev_b32_e32 v170, 16, v171
	v_and_b32_e32 v171, 0xffff0000, v171
	v_lshlrev_b32_e32 v214, 16, v172
	v_and_b32_e32 v215, 0xffff0000, v172
	v_lshlrev_b32_e32 v172, 16, v173
	v_and_b32_e32 v173, 0xffff0000, v173
	v_lshlrev_b32_e32 v216, 16, v174
	v_and_b32_e32 v217, 0xffff0000, v174
	v_lshlrev_b32_e32 v174, 16, v175
	v_and_b32_e32 v175, 0xffff0000, v175
	v_pk_mul_f32 v[192:193], v[126:127], v[192:193]
	v_pk_mul_f32 v[212:213], v[122:123], v[212:213]
	v_pk_mul_f32 v[218:219], v[128:129], v[168:169]
	v_pk_mul_f32 v[220:221], v[124:125], v[170:171]
	v_pk_mul_f32 v[214:215], v[94:95], v[214:215]
	v_pk_mul_f32 v[224:225], v[96:97], v[172:173]
	v_pk_mul_f32 v[216:217], v[90:91], v[216:217]
	v_pk_mul_f32 v[226:227], v[92:93], v[174:175]
	v_cvt_pk_bf16_f32 v168, v192, v193
	v_cvt_pk_bf16_f32 v169, v218, v219
	v_cvt_pk_bf16_f32 v170, v212, v213
	v_cvt_pk_bf16_f32 v171, v220, v221
	v_cvt_pk_bf16_f32 v172, v214, v215
	v_cvt_pk_bf16_f32 v173, v224, v225
	v_cvt_pk_bf16_f32 v174, v216, v217
	v_cvt_pk_bf16_f32 v175, v226, v227
	global_store_dwordx4 v[166:167], v[168:171], off
	global_store_dwordx4 v[166:167], v[172:175], off offset:256
	s_nop 0
	v_lshlrev_b32_e32 v168, 16, v176
	v_and_b32_e32 v169, 0xffff0000, v176
	v_lshlrev_b32_e32 v172, 16, v177
	v_and_b32_e32 v173, 0xffff0000, v177
	v_pk_mul_f32 v[168:169], v[118:119], v[168:169]
	v_lshlrev_b32_e32 v170, 16, v178
	v_and_b32_e32 v171, 0xffff0000, v178
	v_pk_mul_f32 v[172:173], v[120:121], v[172:173]
	v_lshlrev_b32_e32 v174, 16, v179
	v_and_b32_e32 v175, 0xffff0000, v179
	v_pk_mul_f32 v[170:171], v[114:115], v[170:171]
	v_pk_mul_f32 v[174:175], v[116:117], v[174:175]
	v_cvt_pk_bf16_f32 v168, v168, v169
	v_cvt_pk_bf16_f32 v169, v172, v173
	v_add_co_u32_e32 v172, vcc, s56, v166
	v_cvt_pk_bf16_f32 v170, v170, v171
	v_cvt_pk_bf16_f32 v171, v174, v175
	v_addc_co_u32_e32 v173, vcc, 0, v167, vcc
	global_store_dwordx4 v[172:173], v[168:171], off
	s_waitcnt vmcnt(11)
	v_lshlrev_b32_e32 v174, 16, v209
	v_lshlrev_b32_e32 v168, 16, v208
	v_and_b32_e32 v169, 0xffff0000, v208
	v_lshlrev_b32_e32 v170, 16, v210
	v_and_b32_e32 v171, 0xffff0000, v210
	v_and_b32_e32 v175, 0xffff0000, v209
	v_lshlrev_b32_e32 v176, 16, v211
	v_and_b32_e32 v177, 0xffff0000, v211
	v_pk_mul_f32 v[168:169], v[86:87], v[168:169]
	v_pk_mul_f32 v[170:171], v[82:83], v[170:171]
	v_pk_mul_f32 v[174:175], v[88:89], v[174:175]
	v_pk_mul_f32 v[176:177], v[84:85], v[176:177]
	v_cvt_pk_bf16_f32 v168, v168, v169
	v_cvt_pk_bf16_f32 v169, v174, v175
	v_cvt_pk_bf16_f32 v170, v170, v171
	v_cvt_pk_bf16_f32 v171, v176, v177
	global_store_dwordx4 v[172:173], v[168:171], off offset:256
	v_lshlrev_b32_e32 v172, 16, v181
	v_and_b32_e32 v173, 0xffff0000, v181
	v_lshlrev_b32_e32 v168, 16, v180
	v_and_b32_e32 v169, 0xffff0000, v180
	v_pk_mul_f32 v[168:169], v[110:111], v[168:169]
	v_lshlrev_b32_e32 v170, 16, v182
	v_and_b32_e32 v171, 0xffff0000, v182
	v_pk_mul_f32 v[172:173], v[112:113], v[172:173]
	v_lshlrev_b32_e32 v174, 16, v183
	v_and_b32_e32 v175, 0xffff0000, v183
	v_pk_mul_f32 v[170:171], v[106:107], v[170:171]
	v_pk_mul_f32 v[174:175], v[108:109], v[174:175]
	v_cvt_pk_bf16_f32 v168, v168, v169
	v_cvt_pk_bf16_f32 v169, v172, v173
	v_add_co_u32_e32 v172, vcc, s52, v166
	v_cvt_pk_bf16_f32 v170, v170, v171
	v_cvt_pk_bf16_f32 v171, v174, v175
	v_addc_co_u32_e32 v173, vcc, 0, v167, vcc
	global_store_dwordx4 v[172:173], v[168:171], off
	v_lshlrev_b32_e32 v174, 16, v185
	v_and_b32_e32 v175, 0xffff0000, v185
	v_lshlrev_b32_e32 v168, 16, v184
	v_and_b32_e32 v169, 0xffff0000, v184
	v_lshlrev_b32_e32 v170, 16, v186
	v_and_b32_e32 v171, 0xffff0000, v186
	v_lshlrev_b32_e32 v176, 16, v187
	v_and_b32_e32 v177, 0xffff0000, v187
	v_pk_mul_f32 v[168:169], v[78:79], v[168:169]
	v_pk_mul_f32 v[170:171], v[74:75], v[170:171]
	v_pk_mul_f32 v[174:175], v[80:81], v[174:175]
	v_pk_mul_f32 v[176:177], v[76:77], v[176:177]
	v_cvt_pk_bf16_f32 v168, v168, v169
	v_cvt_pk_bf16_f32 v169, v174, v175
	v_cvt_pk_bf16_f32 v170, v170, v171
	v_cvt_pk_bf16_f32 v171, v176, v177
	global_store_dwordx4 v[172:173], v[168:171], off offset:256
	v_lshlrev_b32_e32 v172, 16, v189
	v_and_b32_e32 v173, 0xffff0000, v189
	v_lshlrev_b32_e32 v168, 16, v188
	v_and_b32_e32 v169, 0xffff0000, v188
	v_pk_mul_f32 v[168:169], v[102:103], v[168:169]
	v_lshlrev_b32_e32 v170, 16, v190
	v_and_b32_e32 v171, 0xffff0000, v190
	v_pk_mul_f32 v[172:173], v[104:105], v[172:173]
	v_lshlrev_b32_e32 v174, 16, v191
	v_and_b32_e32 v175, 0xffff0000, v191
	v_pk_mul_f32 v[170:171], v[98:99], v[170:171]
	v_pk_mul_f32 v[174:175], v[100:101], v[174:175]
	v_cvt_pk_bf16_f32 v168, v168, v169
	v_cvt_pk_bf16_f32 v169, v172, v173
	v_add_co_u32_e32 v172, vcc, s55, v166
	v_cvt_pk_bf16_f32 v170, v170, v171
	v_cvt_pk_bf16_f32 v171, v174, v175
	v_addc_co_u32_e32 v173, vcc, 0, v167, vcc
	global_store_dwordx4 v[172:173], v[168:171], off
	s_nop 1
	v_lshlrev_b32_e32 v168, 16, v162
	v_and_b32_e32 v169, 0xffff0000, v162
	v_lshlrev_b32_e32 v162, 16, v163
	v_and_b32_e32 v163, 0xffff0000, v163
	v_lshlrev_b32_e32 v170, 16, v164
	v_and_b32_e32 v171, 0xffff0000, v164
	v_pk_mul_f32 v[174:175], v[72:73], v[162:163]
	v_lshlrev_b32_e32 v162, 16, v165
	v_and_b32_e32 v163, 0xffff0000, v165
	v_pk_mul_f32 v[168:169], v[70:71], v[168:169]
	v_pk_mul_f32 v[170:171], v[66:67], v[170:171]
	v_pk_mul_f32 v[176:177], v[68:69], v[162:163]
	v_cvt_pk_bf16_f32 v162, v168, v169
	v_cvt_pk_bf16_f32 v163, v174, v175
	v_cvt_pk_bf16_f32 v164, v170, v171
	v_cvt_pk_bf16_f32 v165, v176, v177
	global_store_dwordx4 v[172:173], v[162:165], off offset:256
	s_waitcnt vmcnt(15)
	s_nop 0
	v_lshlrev_b32_e32 v162, 16, v158
	v_and_b32_e32 v163, 0xffff0000, v158
	v_lshlrev_b32_e32 v158, 16, v159
	v_and_b32_e32 v159, 0xffff0000, v159
	v_pk_mul_f32 v[162:163], v[62:63], v[162:163]
	v_lshlrev_b32_e32 v164, 16, v160
	v_and_b32_e32 v165, 0xffff0000, v160
	v_pk_mul_f32 v[168:169], v[64:65], v[158:159]
	v_lshlrev_b32_e32 v158, 16, v161
	v_and_b32_e32 v159, 0xffff0000, v161
	v_pk_mul_f32 v[164:165], v[58:59], v[164:165]
	v_pk_mul_f32 v[170:171], v[60:61], v[158:159]
	v_cvt_pk_bf16_f32 v158, v162, v163
	v_add_co_u32_e32 v162, vcc, s57, v166
	v_cvt_pk_bf16_f32 v159, v168, v169
	v_cvt_pk_bf16_f32 v160, v164, v165
	v_cvt_pk_bf16_f32 v161, v170, v171
	v_addc_co_u32_e32 v163, vcc, 0, v167, vcc
	global_store_dwordx4 v[162:163], v[158:161], off
	s_waitcnt vmcnt(15)
	s_nop 0
	v_lshlrev_b32_e32 v158, 16, v154
	v_and_b32_e32 v159, 0xffff0000, v154
	v_lshlrev_b32_e32 v154, 16, v155
	v_and_b32_e32 v155, 0xffff0000, v155
	v_lshlrev_b32_e32 v160, 16, v156
	v_and_b32_e32 v161, 0xffff0000, v156
	v_pk_mul_f32 v[164:165], v[32:33], v[154:155]
	v_lshlrev_b32_e32 v154, 16, v157
	v_and_b32_e32 v155, 0xffff0000, v157
	v_pk_mul_f32 v[158:159], v[30:31], v[158:159]
	v_pk_mul_f32 v[160:161], v[26:27], v[160:161]
	v_pk_mul_f32 v[168:169], v[28:29], v[154:155]
	v_cvt_pk_bf16_f32 v154, v158, v159
	v_cvt_pk_bf16_f32 v155, v164, v165
	v_cvt_pk_bf16_f32 v156, v160, v161
	v_cvt_pk_bf16_f32 v157, v168, v169
	global_store_dwordx4 v[162:163], v[154:157], off offset:256
	s_waitcnt vmcnt(15)
	s_nop 0
	v_lshlrev_b32_e32 v154, 16, v150
	v_and_b32_e32 v155, 0xffff0000, v150
	v_lshlrev_b32_e32 v150, 16, v151
	v_and_b32_e32 v151, 0xffff0000, v151
	v_pk_mul_f32 v[154:155], v[54:55], v[154:155]
	v_lshlrev_b32_e32 v156, 16, v152
	v_and_b32_e32 v157, 0xffff0000, v152
	v_pk_mul_f32 v[158:159], v[56:57], v[150:151]
	v_lshlrev_b32_e32 v150, 16, v153
	v_and_b32_e32 v151, 0xffff0000, v153
	v_pk_mul_f32 v[156:157], v[50:51], v[156:157]
	v_pk_mul_f32 v[160:161], v[52:53], v[150:151]
	v_cvt_pk_bf16_f32 v150, v154, v155
	v_add_co_u32_e32 v154, vcc, s58, v166
	v_cvt_pk_bf16_f32 v151, v158, v159
	v_cvt_pk_bf16_f32 v152, v156, v157
	v_cvt_pk_bf16_f32 v153, v160, v161
	v_addc_co_u32_e32 v155, vcc, 0, v167, vcc
	global_store_dwordx4 v[154:155], v[150:153], off
	s_waitcnt vmcnt(15)
	s_nop 0
	v_lshlrev_b32_e32 v150, 16, v146
	v_and_b32_e32 v151, 0xffff0000, v146
	v_lshlrev_b32_e32 v146, 16, v147
	v_and_b32_e32 v147, 0xffff0000, v147
	v_lshlrev_b32_e32 v152, 16, v148
	v_and_b32_e32 v153, 0xffff0000, v148
	v_pk_mul_f32 v[156:157], v[24:25], v[146:147]
	v_lshlrev_b32_e32 v146, 16, v149
	v_and_b32_e32 v147, 0xffff0000, v149
	v_pk_mul_f32 v[150:151], v[22:23], v[150:151]
	v_pk_mul_f32 v[152:153], v[18:19], v[152:153]
	v_pk_mul_f32 v[158:159], v[20:21], v[146:147]
	v_cvt_pk_bf16_f32 v146, v150, v151
	v_cvt_pk_bf16_f32 v147, v156, v157
	v_cvt_pk_bf16_f32 v148, v152, v153
	v_cvt_pk_bf16_f32 v149, v158, v159
	global_store_dwordx4 v[154:155], v[146:149], off offset:256
	s_waitcnt vmcnt(15)
	s_nop 0
	v_lshlrev_b32_e32 v146, 16, v142
	v_and_b32_e32 v147, 0xffff0000, v142
	v_lshlrev_b32_e32 v142, 16, v143
	v_and_b32_e32 v143, 0xffff0000, v143
	v_pk_mul_f32 v[146:147], v[46:47], v[146:147]
	v_lshlrev_b32_e32 v148, 16, v144
	v_and_b32_e32 v149, 0xffff0000, v144
	v_pk_mul_f32 v[150:151], v[48:49], v[142:143]
	v_lshlrev_b32_e32 v142, 16, v145
	v_and_b32_e32 v143, 0xffff0000, v145
	v_pk_mul_f32 v[148:149], v[42:43], v[148:149]
	v_pk_mul_f32 v[152:153], v[44:45], v[142:143]
	v_cvt_pk_bf16_f32 v142, v146, v147
	v_add_co_u32_e32 v146, vcc, s59, v166
	v_cvt_pk_bf16_f32 v143, v150, v151
	v_cvt_pk_bf16_f32 v144, v148, v149
	v_cvt_pk_bf16_f32 v145, v152, v153
	v_addc_co_u32_e32 v147, vcc, 0, v167, vcc
	global_store_dwordx4 v[146:147], v[142:145], off
	s_waitcnt vmcnt(15)
	s_nop 0
	v_lshlrev_b32_e32 v142, 16, v138
	v_and_b32_e32 v143, 0xffff0000, v138
	v_lshlrev_b32_e32 v138, 16, v139
	v_and_b32_e32 v139, 0xffff0000, v139
	v_lshlrev_b32_e32 v144, 16, v140
	v_and_b32_e32 v145, 0xffff0000, v140
	v_pk_mul_f32 v[148:149], v[16:17], v[138:139]
	v_lshlrev_b32_e32 v138, 16, v141
	v_and_b32_e32 v139, 0xffff0000, v141
	v_pk_mul_f32 v[142:143], v[14:15], v[142:143]
	v_pk_mul_f32 v[144:145], v[10:11], v[144:145]
	v_pk_mul_f32 v[150:151], v[12:13], v[138:139]
	v_cvt_pk_bf16_f32 v138, v142, v143
	v_cvt_pk_bf16_f32 v139, v148, v149
	v_cvt_pk_bf16_f32 v140, v144, v145
	v_cvt_pk_bf16_f32 v141, v150, v151
	global_store_dwordx4 v[146:147], v[138:141], off offset:256
	s_waitcnt vmcnt(15)
	s_nop 0
	v_lshlrev_b32_e32 v138, 16, v134
	v_and_b32_e32 v139, 0xffff0000, v134
	v_lshlrev_b32_e32 v134, 16, v135
	v_and_b32_e32 v135, 0xffff0000, v135
	v_pk_mul_f32 v[138:139], v[38:39], v[138:139]
	v_lshlrev_b32_e32 v140, 16, v136
	v_and_b32_e32 v141, 0xffff0000, v136
	v_pk_mul_f32 v[142:143], v[40:41], v[134:135]
	v_lshlrev_b32_e32 v134, 16, v137
	v_and_b32_e32 v135, 0xffff0000, v137
	v_pk_mul_f32 v[140:141], v[34:35], v[140:141]
	v_pk_mul_f32 v[144:145], v[36:37], v[134:135]
	v_cvt_pk_bf16_f32 v134, v138, v139
	v_add_co_u32_e32 v138, vcc, s60, v166
	v_cvt_pk_bf16_f32 v135, v142, v143
	v_cvt_pk_bf16_f32 v136, v140, v141
	v_cvt_pk_bf16_f32 v137, v144, v145
	v_addc_co_u32_e32 v139, vcc, 0, v167, vcc
	global_store_dwordx4 v[138:139], v[134:137], off
	s_andn2_b64 vcc, exec, s[16:17]
	s_mov_b64 s[16:17], -1
	s_waitcnt vmcnt(15)
	v_lshlrev_b32_e32 v134, 16, v130
	v_and_b32_e32 v135, 0xffff0000, v130
	v_lshlrev_b32_e32 v130, 16, v131
	v_and_b32_e32 v131, 0xffff0000, v131
	v_lshlrev_b32_e32 v136, 16, v132
	v_and_b32_e32 v137, 0xffff0000, v132
	v_pk_mul_f32 v[140:141], v[8:9], v[130:131]
	v_lshlrev_b32_e32 v130, 16, v133
	v_and_b32_e32 v131, 0xffff0000, v133
	v_pk_mul_f32 v[134:135], v[6:7], v[134:135]
	v_pk_mul_f32 v[136:137], v[2:3], v[136:137]
	v_pk_mul_f32 v[142:143], v[4:5], v[130:131]
	v_cvt_pk_bf16_f32 v130, v134, v135
	v_cvt_pk_bf16_f32 v131, v140, v141
	v_cvt_pk_bf16_f32 v132, v136, v137
	v_cvt_pk_bf16_f32 v133, v142, v143
	global_store_dwordx4 v[138:139], v[130:133], off offset:256
	s_cbranch_vccnz .LBB0_755
	s_andn2_b64 vcc, exec, s[0:1]
	s_cbranch_vccnz .LBB0_754
	s_barrier
	s_branch .LBB0_754
